# masked attention step-end wait leaves the next mask load in flight (vmcnt(1)); it is consumed behind the next step's own wait
# baseline (speedup 1.0000x reference)
; #define LDS_WAIT() asm volatile("s_waitcnt lgkmcnt(0)" ::: "memory")
; __device__ __forceinline__ int crow(int r, int hi) { return (r & 3) + 8 * (r >> 2) + 4 * hi; }
; __device__ __forceinline__ void dsa_step(f32x16& c0, f32x16& c1, f32x16& n0, f32x16& n1, const bool have_n, const LAS char* kpn, const LAS char* vpc, const bf16x8 (&qr)[4], unsigned long long mwn, ...
;     ...
;     f32x2 ps2 = {0.f, 0.f};
; #pragma unroll
;     for (int r = 0; r < 16; r += 2) { c0[r] = __builtin_amdgcn_exp2f(c0[r]); c0[r + 1] = __builtin_amdgcn_exp2f(c0[r + 1]); c1[r] = __builtin_amdgcn_exp2f(c1[r]); c1[r + 1] = __builtin_amdgcn_exp2f(c1[r + 1]);
;         ps2 += (f32x2){c0[r], c0[r + 1]}; ps2 += (f32x2){c1[r], c1[r + 1]}; }
;     lsum += ps2[0] + ps2[1];
;     if (resc) { LDS_WAIT();
; #pragma unroll
;         for (int r = 0; r < 16; ++r) { const float f = wsf[crow(r, hi)]; o[0][r] *= f; o[1][r] *= f; } }
;     pv_mma(o, vf, c0, c1);
;     asm volatile("s_waitcnt vmcnt(0) lgkmcnt(0)\n\ts_barrier" ::: "memory");
; __device__ __forceinline__ void dsa_block_unit(int b, int g, int m  , const bf16_t* Q, const bf16_t* K, const bf16_t* V, const unsigned long long* mask, bf16_t* O, LAS char* L, int wid, int lane, float sbound  ) {
;     ...
;         { const int t_ = sc; sc = sn; sn = sn2; sn2 = t_; } mwn = mwn2;
;         if (j + 3 <= jd) { glds16_s(Kw + (size_t)(j + 3) * 64 * 128, kvoff, kdst + sn2); glds16_s(Vw + (size_t)(j + 3) * 64 * 128, vvoff, vdst + sn2); mwn2 = mrow[j + 3]; }
.LBB0_1696:
	s_or_b64 exec, exec, s[34:35]
	v_exp_f32_e32 v34, v34
	v_exp_f32_e32 v35, v35
	v_exp_f32_e32 v36, v36
	v_exp_f32_e32 v37, v37
	v_exp_f32_e32 v38, v38
	v_exp_f32_e32 v39, v39
	v_exp_f32_e32 v40, v40
	v_exp_f32_e32 v41, v41
	v_cvt_pk_bf16_f32 v146, v34, v35
	v_cvt_pk_bf16_f32 v147, v36, v37
	v_cvt_pk_bf16_f32 v148, v38, v39
	v_cvt_pk_bf16_f32 v149, v40, v41
	v_exp_f32_e32 v42, v42
	v_exp_f32_e32 v43, v43
	v_exp_f32_e32 v44, v44
	v_exp_f32_e32 v45, v45
	v_exp_f32_e32 v46, v46
	v_exp_f32_e32 v47, v47
	v_exp_f32_e32 v48, v48
	v_exp_f32_e32 v49, v49
	s_waitcnt lgkmcnt(14)
	v_mfma_f32_32x32x16_bf16 v[2:17], v[146:149], v[142:145], v[2:17]
	v_exp_f32_e32 v50, v50
	v_exp_f32_e32 v51, v51
	v_cvt_pk_bf16_f32 v142, v42, v43
	v_cvt_pk_bf16_f32 v143, v44, v45
	v_cvt_pk_bf16_f32 v144, v46, v47
	v_cvt_pk_bf16_f32 v145, v48, v49
	v_exp_f32_e32 v52, v52
	s_waitcnt lgkmcnt(10)
	v_mfma_f32_32x32x16_bf16 v[18:33], v[146:149], v[138:141], v[18:33]
	v_exp_f32_e32 v53, v53
	v_pk_add_f32 v[186:187], v[34:35], 0 op_sel_hi:[1,0]
	v_exp_f32_e32 v54, v54
	v_pk_add_f32 v[186:187], v[50:51], v[186:187]
	v_exp_f32_e32 v55, v55
	v_exp_f32_e32 v56, v56
	v_exp_f32_e32 v57, v57
	v_mfma_f32_32x32x16_bf16 v[2:17], v[142:145], v[134:137], v[2:17]
	v_add_f32_e64 v134, v186, v36
	v_add_f32_e64 v135, v187, v37
	v_cvt_pk_bf16_f32 v136, v54, v55
	v_add_f32_e64 v134, v52, v134
	v_add_f32_e64 v135, v53, v135
	v_cvt_pk_bf16_f32 v137, v56, v57
	v_pk_add_f32 v[134:135], v[134:135], v[38:39]
	v_exp_f32_e32 v58, v58
	v_pk_add_f32 v[138:139], v[54:55], v[134:135]
	s_waitcnt lgkmcnt(8)
	v_mfma_f32_32x32x16_bf16 v[18:33], v[142:145], v[130:133], v[18:33]
	v_cvt_pk_bf16_f32 v134, v50, v51
	v_cvt_pk_bf16_f32 v135, v52, v53
	v_exp_f32_e32 v59, v59
	v_exp_f32_e32 v60, v60
	v_exp_f32_e32 v61, v61
	v_exp_f32_e32 v62, v62
	v_exp_f32_e32 v63, v63
	v_exp_f32_e32 v64, v64
	v_exp_f32_e32 v65, v65
	s_waitcnt lgkmcnt(6)
	v_mfma_f32_32x32x16_bf16 v[2:17], v[134:137], v[126:129], v[2:17]
	v_cvt_pk_bf16_f32 v126, v58, v59
	v_cvt_pk_bf16_f32 v127, v60, v61
	v_cvt_pk_bf16_f32 v128, v62, v63
	v_cvt_pk_bf16_f32 v129, v64, v65
	v_add_f32_e64 v130, v138, v40
	v_add_f32_e64 v131, v139, v41
	s_waitcnt vmcnt(1) lgkmcnt(0)
	s_barrier
	s_add_i32 s0, s21, s58
	s_waitcnt lgkmcnt(2)
	v_mfma_f32_32x32x16_bf16 v[18:33], v[134:137], v[122:125], v[18:33]
	v_add_f32_e64 v130, v56, v130
	v_add_f32_e64 v131, v57, v131
	s_cmp_eq_u32 s0, 3
	v_add_f32_e64 v122, v130, v42
	v_add_f32_e64 v123, v131, v43
	v_readfirstlane_b32 s36, v0
	v_pk_add_f32 v[122:123], v[58:59], v[122:123]
	v_readfirstlane_b32 s37, v1
	v_pk_add_f32 v[122:123], v[122:123], v[44:45]
	v_mfma_f32_32x32x16_bf16 v[2:17], v[126:129], v[118:121], v[2:17]
	v_add_f32_e64 v122, v60, v122
	v_add_f32_e64 v123, v61, v123
	v_add_f32_e64 v118, v122, v46
	v_add_f32_e64 v119, v123, v47
	v_add_f32_e64 v118, v62, v118
	v_add_f32_e64 v119, v63, v119
	v_pk_add_f32 v[118:119], v[118:119], v[48:49]
	s_waitcnt lgkmcnt(0)
	v_mfma_f32_32x32x16_bf16 v[18:33], v[126:129], v[114:117], v[18:33]
	v_add_f32_e64 v118, v64, v118
	v_add_f32_e64 v119, v65, v119
	v_add_f32_e32 v118, v118, v119
	v_add_f32_e32 v157, v157, v118
	s_cbranch_scc1 .LBB0_1682
	s_cmp_gt_u32 s58, s54
	s_waitcnt vmcnt(0)
	v_mov_b64_e32 v[116:117], v[170:171]
	s_cbranch_scc1 .LBB0_1699
	s_add_u32 s0, s16, s30
	s_addc_u32 s1, s17, s31
	s_add_u32 s0, s0, 0xc000
	s_addc_u32 s1, s1, 0
	s_add_i32 s33, s55, s63
	s_add_u32 s2, s18, s30
	s_addc_u32 s3, s19, s31
	s_add_u32 s2, s2, 0xc000
	s_mov_b32 s35, m0
	s_mov_b32 m0, s33
	s_nop 0
	global_load_lds_dwordx4 v172, s[0:1]
	s_mov_b32 m0, s35
	s_addc_u32 s3, s3, 0
	s_add_i32 s34, s55, s64
	s_mov_b32 s0, m0
	s_mov_b32 m0, s34
	s_nop 0
	global_load_lds_dwordx4 v173, s[2:3]
	s_mov_b32 m0, s0
	global_load_dwordx2 v[116:117], v[168:169], off sc1

; #define LDS_WAIT() asm volatile("s_waitcnt lgkmcnt(0)" ::: "memory")
; __device__ __forceinline__ int crow(int r, int hi) { return (r & 3) + 8 * (r >> 2) + 4 * hi; }
; __device__ __forceinline__ void dsa_step(f32x16& c0, f32x16& c1, f32x16& n0, f32x16& n1, const bool have_n, const LAS char* kpn, const LAS char* vpc, const bf16x8 (&qr)[4], unsigned long long mwn, ...
;     ...
;     f32x2 ps2 = {0.f, 0.f};
; #pragma unroll
;     for (int r = 0; r < 16; r += 2) { c0[r] = __builtin_amdgcn_exp2f(c0[r]); c0[r + 1] = __builtin_amdgcn_exp2f(c0[r + 1]); c1[r] = __builtin_amdgcn_exp2f(c1[r]); c1[r + 1] = __builtin_amdgcn_exp2f(c1[r + 1]);
;         ps2 += (f32x2){c0[r], c0[r + 1]}; ps2 += (f32x2){c1[r], c1[r + 1]}; }
;     lsum += ps2[0] + ps2[1];
;     if (resc) { LDS_WAIT();
; #pragma unroll
;         for (int r = 0; r < 16; ++r) { const float f = wsf[crow(r, hi)]; o[0][r] *= f; o[1][r] *= f; } }
;     pv_mma(o, vf, c0, c1);
;     asm volatile("s_waitcnt vmcnt(0) lgkmcnt(0)\n\ts_barrier" ::: "memory");
; __device__ __forceinline__ void dsa_block_unit(int b, int g, int m  , const bf16_t* Q, const bf16_t* K, const bf16_t* V, const unsigned long long* mask, bf16_t* O, LAS char* L, int wid, int lane, float sbound  ) {
;     ...
;         dsa_step(pb0, pb1, pa0, pa1, j + 1 < jd, kp0 + sn, vp0 + sc, qr, mwn, o, mref, lsum, wsf, r32, hi, fixed, tblp);
;         { const int t_ = sc; sc = sn; sn = sn2; sn2 = t_; } mwn = mwn2;
.LBB0_1709:
	s_or_b64 exec, exec, s[34:35]
	v_exp_f32_e32 v82, v82
	v_exp_f32_e32 v83, v83
	v_exp_f32_e32 v84, v84
	v_exp_f32_e32 v85, v85
	v_exp_f32_e32 v86, v86
	v_exp_f32_e32 v87, v87
	v_exp_f32_e32 v88, v88
	v_exp_f32_e32 v89, v89
	v_cvt_pk_bf16_f32 v186, v82, v83
	v_cvt_pk_bf16_f32 v187, v84, v85
	v_cvt_pk_bf16_f32 v188, v86, v87
	v_cvt_pk_bf16_f32 v189, v88, v89
	v_exp_f32_e32 v90, v90
	v_exp_f32_e32 v91, v91
	v_exp_f32_e32 v92, v92
	v_exp_f32_e32 v93, v93
	v_exp_f32_e32 v94, v94
	v_exp_f32_e32 v95, v95
	v_exp_f32_e32 v96, v96
	v_exp_f32_e32 v97, v97
	s_waitcnt lgkmcnt(14)
	v_mfma_f32_32x32x16_bf16 v[2:17], v[186:189], v[146:149], v[2:17]
	v_cvt_pk_bf16_f32 v146, v90, v91
	v_cvt_pk_bf16_f32 v147, v92, v93
	v_cvt_pk_bf16_f32 v148, v94, v95
	v_cvt_pk_bf16_f32 v149, v96, v97
	v_exp_f32_e32 v66, v66
	v_exp_f32_e32 v67, v67
	v_exp_f32_e32 v68, v68
	s_waitcnt lgkmcnt(10)
	v_mfma_f32_32x32x16_bf16 v[18:33], v[186:189], v[142:145], v[18:33]
	v_exp_f32_e32 v69, v69
	v_exp_f32_e32 v70, v70
	v_exp_f32_e32 v71, v71
	v_exp_f32_e32 v72, v72
	v_exp_f32_e32 v73, v73
	v_pk_add_f32 v[114:115], v[82:83], 0 op_sel_hi:[1,0]
	v_exp_f32_e32 v74, v74
	v_mfma_f32_32x32x16_bf16 v[2:17], v[146:149], v[138:141], v[2:17]
	v_cvt_pk_bf16_f32 v138, v66, v67
	v_cvt_pk_bf16_f32 v139, v68, v69
	v_cvt_pk_bf16_f32 v140, v70, v71
	v_cvt_pk_bf16_f32 v141, v72, v73
	v_add_f32_e64 v114, v66, v114
	v_add_f32_e64 v115, v67, v115
	v_exp_f32_e32 v75, v75
	v_exp_f32_e32 v76, v76
	s_waitcnt lgkmcnt(8)
	v_mfma_f32_32x32x16_bf16 v[18:33], v[146:149], v[134:137], v[18:33]
	v_exp_f32_e32 v77, v77
	v_exp_f32_e32 v78, v78
	v_exp_f32_e32 v79, v79
	v_exp_f32_e32 v80, v80
	v_exp_f32_e32 v81, v81
	v_pk_add_f32 v[114:115], v[114:115], v[84:85]
	s_add_u32 s30, s30, 0x8000
	s_waitcnt lgkmcnt(6)
	v_mfma_f32_32x32x16_bf16 v[2:17], v[138:141], v[130:133], v[2:17]
	v_add_f32_e64 v114, v68, v114
	v_add_f32_e64 v115, v69, v115
	v_cvt_pk_bf16_f32 v130, v74, v75
	v_add_f32_e64 v114, v114, v86
	v_add_f32_e64 v115, v115, v87
	v_cvt_pk_bf16_f32 v131, v76, v77
	v_pk_add_f32 v[114:115], v[70:71], v[114:115]
	v_cvt_pk_bf16_f32 v132, v78, v79
	v_cvt_pk_bf16_f32 v133, v80, v81
	s_waitcnt lgkmcnt(2)
	v_mfma_f32_32x32x16_bf16 v[18:33], v[138:141], v[126:129], v[18:33]
	v_add_f32_e64 v114, v114, v88
	v_add_f32_e64 v115, v115, v89
	s_waitcnt vmcnt(1) lgkmcnt(0)
	s_barrier
	s_addc_u32 s31, s31, 0
	v_add_f32_e64 v114, v72, v114
	v_add_f32_e64 v115, v73, v115
	s_add_i32 s58, s58, 2
	v_pk_add_f32 v[114:115], v[114:115], v[90:91]
	s_cmp_gt_u32 s60, s54
	v_pk_add_f32 v[114:115], v[74:75], v[114:115]
	v_mfma_f32_32x32x16_bf16 v[2:17], v[130:133], v[122:125], v[2:17]
	v_add_f32_e64 v114, v114, v92
	v_add_f32_e64 v115, v115, v93
	v_lshl_add_u64 v[168:169], v[168:169], 0, 16
	v_add_f32_e64 v114, v76, v114
	v_add_f32_e64 v115, v77, v115
	s_cselect_b64 s[34:35], -1, 0
	v_pk_add_f32 v[114:115], v[114:115], v[94:95]
	s_nop 0
	v_pk_add_f32 v[114:115], v[78:79], v[114:115]
	s_waitcnt lgkmcnt(0)
	v_mfma_f32_32x32x16_bf16 v[18:33], v[130:133], v[118:121], v[18:33]
	v_add_f32_e64 v114, v114, v96
	v_add_f32_e64 v115, v115, v97
	v_add_f32_e64 v114, v80, v114
	v_add_f32_e64 v115, v81, v115
	v_add_f32_e32 v114, v114, v115
	v_add_f32_e32 v157, v157, v114
	s_branch .LBB0_1683

; #define LDS_WAIT() asm volatile("s_waitcnt lgkmcnt(0)" ::: "memory")
; __device__ __forceinline__ int crow(int r, int hi) { return (r & 3) + 8 * (r >> 2) + 4 * hi; }
; __device__ __forceinline__ void dsa_step(f32x16& c0, f32x16& c1, f32x16& n0, f32x16& n1, const bool have_n, const LAS char* kpn, const LAS char* vpc, const bf16x8 (&qr)[4], unsigned long long mwn, ...
;     ...
;     f32x2 ps2 = {0.f, 0.f};
; #pragma unroll
;     for (int r = 0; r < 16; r += 2) { c0[r] = __builtin_amdgcn_exp2f(c0[r]); c0[r + 1] = __builtin_amdgcn_exp2f(c0[r + 1]); c1[r] = __builtin_amdgcn_exp2f(c1[r]); c1[r + 1] = __builtin_amdgcn_exp2f(c1[r + 1]);
;         ps2 += (f32x2){c0[r], c0[r + 1]}; ps2 += (f32x2){c1[r], c1[r + 1]}; }
;     lsum += ps2[0] + ps2[1];
;     if (resc) { LDS_WAIT();
; #pragma unroll
;         for (int r = 0; r < 16; ++r) { const float f = wsf[crow(r, hi)]; o[0][r] *= f; o[1][r] *= f; } }
;     pv_mma(o, vf, c0, c1);
;     asm volatile("s_waitcnt vmcnt(0) lgkmcnt(0)\n\ts_barrier" ::: "memory");
; __device__ __forceinline__ void dsa_block_unit(int b, int g, int m  , const bf16_t* Q, const bf16_t* K, const bf16_t* V, const unsigned long long* mask, bf16_t* O, LAS char* L, int wid, int lane, float sbound  ) {
;     ...
;         { const int t_ = sc; sc = sn; sn = sn2; sn2 = t_; } mwn = mwn2;
;         if (j + 3 <= jd) { glds16_s(Kw + (size_t)(j + 3) * 64 * 128, kvoff, kdst + sn2); glds16_s(Vw + (size_t)(j + 3) * 64 * 128, vvoff, vdst + sn2); mwn2 = mrow[j + 3]; }
.LBB0_1767:
	s_or_b64 exec, exec, s[22:23]
	v_exp_f32_e32 v34, v34
	v_exp_f32_e32 v35, v35
	v_exp_f32_e32 v36, v36
	v_exp_f32_e32 v37, v37
	v_exp_f32_e32 v38, v38
	v_exp_f32_e32 v39, v39
	v_exp_f32_e32 v40, v40
	v_exp_f32_e32 v41, v41
	v_cvt_pk_bf16_f32 v186, v34, v35
	v_cvt_pk_bf16_f32 v187, v36, v37
	v_cvt_pk_bf16_f32 v188, v38, v39
	v_cvt_pk_bf16_f32 v189, v40, v41
	v_exp_f32_e32 v42, v42
	v_exp_f32_e32 v43, v43
	v_exp_f32_e32 v44, v44
	v_exp_f32_e32 v45, v45
	v_exp_f32_e32 v46, v46
	v_exp_f32_e32 v47, v47
	v_exp_f32_e32 v48, v48
	v_exp_f32_e32 v49, v49
	s_waitcnt lgkmcnt(14)
	v_mfma_f32_32x32x16_bf16 v[18:33], v[186:189], v[142:145], v[18:33]
	v_exp_f32_e32 v50, v50
	v_exp_f32_e32 v51, v51
	v_cvt_pk_bf16_f32 v142, v42, v43
	v_cvt_pk_bf16_f32 v143, v44, v45
	v_cvt_pk_bf16_f32 v144, v46, v47
	v_cvt_pk_bf16_f32 v145, v48, v49
	v_exp_f32_e32 v52, v52
	s_waitcnt lgkmcnt(10)
	v_mfma_f32_32x32x16_bf16 v[2:17], v[186:189], v[138:141], v[2:17]
	v_exp_f32_e32 v53, v53
	v_pk_add_f32 v[148:149], v[34:35], 0 op_sel_hi:[1,0]
	v_exp_f32_e32 v54, v54
	v_pk_add_f32 v[148:149], v[50:51], v[148:149]
	v_exp_f32_e32 v55, v55
	v_exp_f32_e32 v56, v56
	v_exp_f32_e32 v57, v57
	v_mfma_f32_32x32x16_bf16 v[18:33], v[142:145], v[134:137], v[18:33]
	v_add_f32_e64 v134, v148, v36
	v_add_f32_e64 v135, v149, v37
	v_cvt_pk_bf16_f32 v136, v54, v55
	v_add_f32_e64 v134, v52, v134
	v_add_f32_e64 v135, v53, v135
	v_cvt_pk_bf16_f32 v137, v56, v57
	v_pk_add_f32 v[134:135], v[134:135], v[38:39]
	v_exp_f32_e32 v58, v58
	v_pk_add_f32 v[138:139], v[54:55], v[134:135]
	s_waitcnt lgkmcnt(8)
	v_mfma_f32_32x32x16_bf16 v[2:17], v[142:145], v[130:133], v[2:17]
	v_cvt_pk_bf16_f32 v134, v50, v51
	v_cvt_pk_bf16_f32 v135, v52, v53
	v_exp_f32_e32 v59, v59
	v_exp_f32_e32 v60, v60
	v_exp_f32_e32 v61, v61
	v_exp_f32_e32 v62, v62
	v_exp_f32_e32 v63, v63
	v_exp_f32_e32 v64, v64
	v_exp_f32_e32 v65, v65
	s_waitcnt lgkmcnt(6)
	v_mfma_f32_32x32x16_bf16 v[18:33], v[134:137], v[126:129], v[18:33]
	v_cvt_pk_bf16_f32 v126, v58, v59
	v_cvt_pk_bf16_f32 v127, v60, v61
	v_cvt_pk_bf16_f32 v128, v62, v63
	v_cvt_pk_bf16_f32 v129, v64, v65
	v_add_f32_e64 v130, v138, v40
	v_add_f32_e64 v131, v139, v41
	s_waitcnt vmcnt(1) lgkmcnt(0)
	s_barrier
	s_add_i32 s0, s30, s35
	s_waitcnt lgkmcnt(2)
	v_mfma_f32_32x32x16_bf16 v[2:17], v[134:137], v[122:125], v[2:17]
	v_add_f32_e64 v130, v56, v130
	v_add_f32_e64 v131, v57, v131
	s_cmp_eq_u32 s0, 3
	v_add_f32_e64 v122, v130, v42
	v_add_f32_e64 v123, v131, v43
	v_readfirstlane_b32 s25, v1
	v_pk_add_f32 v[122:123], v[58:59], v[122:123]
	s_nop 0
	v_pk_add_f32 v[122:123], v[122:123], v[44:45]
	v_mfma_f32_32x32x16_bf16 v[18:33], v[126:129], v[118:121], v[18:33]
	v_add_f32_e64 v122, v60, v122
	v_add_f32_e64 v123, v61, v123
	v_add_f32_e64 v118, v122, v46
	v_add_f32_e64 v119, v123, v47
	v_add_f32_e64 v118, v62, v118
	v_add_f32_e64 v119, v63, v119
	v_pk_add_f32 v[118:119], v[118:119], v[48:49]
	s_waitcnt lgkmcnt(0)
	v_mfma_f32_32x32x16_bf16 v[2:17], v[126:129], v[114:117], v[2:17]
	v_add_f32_e64 v118, v64, v118
	v_add_f32_e64 v119, v65, v119
	v_add_f32_e32 v0, v118, v119
	v_add_f32_e32 v157, v157, v0
	v_readfirstlane_b32 s24, v0
	s_cbranch_scc1 .LBB0_1753
	s_cmp_gt_u32 s35, s53
	s_waitcnt vmcnt(0)
	v_mov_b64_e32 v[148:149], v[166:167]
	s_cbranch_scc1 .LBB0_1770
	s_add_u32 s0, s16, s20
	s_addc_u32 s1, s17, s21
	s_add_u32 s0, s0, 0xc000
	s_addc_u32 s1, s1, 0
	s_add_i32 s22, s31, s63
	s_add_u32 s2, s18, s20
	s_addc_u32 s3, s19, s21
	s_add_u32 s2, s2, 0xc000
	s_mov_b32 s24, m0
	s_mov_b32 m0, s22
	s_nop 0
	global_load_lds_dwordx4 v172, s[0:1]
	s_mov_b32 m0, s24
	s_addc_u32 s3, s3, 0
	s_add_i32 s23, s31, s64
	s_mov_b32 s0, m0
	s_mov_b32 m0, s23
	s_nop 0
	global_load_lds_dwordx4 v173, s[2:3]
	s_mov_b32 m0, s0
	global_load_dwordx2 v[148:149], v[146:147], off sc1

; #define LDS_WAIT() asm volatile("s_waitcnt lgkmcnt(0)" ::: "memory")
; __device__ __forceinline__ int crow(int r, int hi) { return (r & 3) + 8 * (r >> 2) + 4 * hi; }
; __device__ __forceinline__ void dsa_step(f32x16& c0, f32x16& c1, f32x16& n0, f32x16& n1, const bool have_n, const LAS char* kpn, const LAS char* vpc, const bf16x8 (&qr)[4], unsigned long long mwn, ...
;     ...
;     f32x2 ps2 = {0.f, 0.f};
; #pragma unroll
;     for (int r = 0; r < 16; r += 2) { c0[r] = __builtin_amdgcn_exp2f(c0[r]); c0[r + 1] = __builtin_amdgcn_exp2f(c0[r + 1]); c1[r] = __builtin_amdgcn_exp2f(c1[r]); c1[r + 1] = __builtin_amdgcn_exp2f(c1[r + 1]);
;         ps2 += (f32x2){c0[r], c0[r + 1]}; ps2 += (f32x2){c1[r], c1[r + 1]}; }
;     lsum += ps2[0] + ps2[1];
;     if (resc) { LDS_WAIT();
; #pragma unroll
;         for (int r = 0; r < 16; ++r) { const float f = wsf[crow(r, hi)]; o[0][r] *= f; o[1][r] *= f; } }
;     pv_mma(o, vf, c0, c1);
;     asm volatile("s_waitcnt vmcnt(0) lgkmcnt(0)\n\ts_barrier" ::: "memory");
; __device__ __forceinline__ void dsa_block_unit(int b, int g, int m  , const bf16_t* Q, const bf16_t* K, const bf16_t* V, const unsigned long long* mask, bf16_t* O, LAS char* L, int wid, int lane, float sbound  ) {
;     ...
;         dsa_step(pb0, pb1, pa0, pa1, j + 1 < jd, kp0 + sn, vp0 + sc, qr, mwn, o, mref, lsum, wsf, r32, hi, fixed, tblp);
;         { const int t_ = sc; sc = sn; sn = sn2; sn2 = t_; } mwn = mwn2;
.LBB0_1780:
	s_or_b64 exec, exec, s[22:23]
	v_exp_f32_e32 v82, v82
	v_exp_f32_e32 v83, v83
	v_exp_f32_e32 v84, v84
	v_exp_f32_e32 v85, v85
	v_exp_f32_e32 v86, v86
	v_exp_f32_e32 v87, v87
	v_exp_f32_e32 v88, v88
	v_exp_f32_e32 v89, v89
	v_cvt_pk_bf16_f32 v186, v82, v83
	v_cvt_pk_bf16_f32 v187, v84, v85
	v_cvt_pk_bf16_f32 v188, v86, v87
	v_cvt_pk_bf16_f32 v189, v88, v89
	v_exp_f32_e32 v90, v90
	v_exp_f32_e32 v91, v91
	v_exp_f32_e32 v92, v92
	v_exp_f32_e32 v93, v93
	v_exp_f32_e32 v94, v94
	v_exp_f32_e32 v95, v95
	v_exp_f32_e32 v96, v96
	v_exp_f32_e32 v97, v97
	s_waitcnt lgkmcnt(14)
	v_mfma_f32_32x32x16_bf16 v[18:33], v[186:189], v[142:145], v[18:33]
	v_cvt_pk_bf16_f32 v142, v90, v91
	v_cvt_pk_bf16_f32 v143, v92, v93
	v_cvt_pk_bf16_f32 v144, v94, v95
	v_cvt_pk_bf16_f32 v145, v96, v97
	v_exp_f32_e32 v66, v66
	v_exp_f32_e32 v67, v67
	v_exp_f32_e32 v68, v68
	s_waitcnt lgkmcnt(10)
	v_mfma_f32_32x32x16_bf16 v[2:17], v[186:189], v[138:141], v[2:17]
	v_exp_f32_e32 v69, v69
	v_pk_add_f32 v[166:167], v[82:83], 0 op_sel_hi:[1,0]
	v_exp_f32_e32 v70, v70
	v_exp_f32_e32 v71, v71
	v_exp_f32_e32 v72, v72
	v_exp_f32_e32 v73, v73
	v_pk_add_f32 v[138:139], v[66:67], v[166:167]
	v_mfma_f32_32x32x16_bf16 v[18:33], v[142:145], v[134:137], v[18:33]
	v_add_f32_e64 v138, v138, v84
	v_add_f32_e64 v139, v139, v85
	v_cvt_pk_bf16_f32 v136, v70, v71
	v_add_f32_e64 v134, v68, v138
	v_add_f32_e64 v135, v69, v139
	v_cvt_pk_bf16_f32 v137, v72, v73
	v_pk_add_f32 v[138:139], v[134:135], v[86:87]
	v_cvt_pk_bf16_f32 v134, v66, v67
	v_cvt_pk_bf16_f32 v135, v68, v69
	s_waitcnt lgkmcnt(8)
	v_mfma_f32_32x32x16_bf16 v[2:17], v[142:145], v[130:133], v[2:17]
	v_exp_f32_e32 v74, v74
	v_exp_f32_e32 v75, v75
	v_exp_f32_e32 v76, v76
	v_exp_f32_e32 v77, v77
	v_exp_f32_e32 v78, v78
	v_exp_f32_e32 v79, v79
	v_exp_f32_e32 v80, v80
	v_exp_f32_e32 v81, v81
	s_waitcnt lgkmcnt(6)
	v_mfma_f32_32x32x16_bf16 v[18:33], v[134:137], v[126:129], v[18:33]
	v_add_f32_e64 v130, v70, v138
	v_add_f32_e64 v131, v71, v139
	v_cvt_pk_bf16_f32 v126, v74, v75
	v_cvt_pk_bf16_f32 v127, v76, v77
	v_cvt_pk_bf16_f32 v128, v78, v79
	v_cvt_pk_bf16_f32 v129, v80, v81
	v_pk_add_f32 v[130:131], v[130:131], v[88:89]
	s_add_u32 s20, s20, 0x8000
	s_waitcnt lgkmcnt(2)
	v_mfma_f32_32x32x16_bf16 v[2:17], v[134:137], v[122:125], v[2:17]
	v_add_f32_e64 v122, v72, v130
	v_add_f32_e64 v123, v73, v131
	s_waitcnt vmcnt(1) lgkmcnt(0)
	s_barrier
	s_addc_u32 s21, s21, 0
	v_add_f32_e64 v122, v122, v90
	v_add_f32_e64 v123, v123, v91
	s_add_i32 s35, s35, 2
	v_pk_add_f32 v[122:123], v[74:75], v[122:123]
	s_cmp_gt_u32 s37, s53
	v_pk_add_f32 v[122:123], v[122:123], v[92:93]
	v_mfma_f32_32x32x16_bf16 v[18:33], v[126:129], v[118:121], v[18:33]
	v_add_f32_e64 v118, v76, v122
	v_add_f32_e64 v119, v77, v123
	v_lshl_add_u64 v[146:147], v[146:147], 0, 16
	v_add_f32_e64 v118, v118, v94
	v_add_f32_e64 v119, v119, v95
	s_cselect_b64 s[22:23], -1, 0
	v_pk_add_f32 v[118:119], v[78:79], v[118:119]
	s_nop 0
	v_pk_add_f32 v[118:119], v[118:119], v[96:97]
	s_waitcnt lgkmcnt(0)
	v_mfma_f32_32x32x16_bf16 v[2:17], v[126:129], v[114:117], v[2:17]
	v_add_f32_e64 v118, v80, v118
	v_add_f32_e64 v119, v81, v119
	v_add_f32_e32 v0, v118, v119
	v_add_f32_e32 v157, v157, v0
	s_branch .LBB0_1754
